# grid barrier: L1 invalidate issued right after the arrival atomic returns (overlaps the wait for release) instead of after the release is observed (on v16)
# speedup vs baseline: 1.0135x; 1.0068x over previous
.LBB0_87:
	s_or_b64 exec, exec, s[28:29]
	v_cvt_f32_u32_e32 v5, v3
	s_waitcnt vmcnt(0)
	buffer_inv sc1
	v_readfirstlane_b32 s4, v4
	v_sub_u32_e32 v4, 0, v3
	v_rcp_iflag_f32_e32 v5, v5
	v_add_u32_e32 v6, s4, v1
	v_mul_f32_e32 v5, 0x4f7ffffe, v5
	v_cvt_u32_f32_e32 v5, v5
	v_mul_lo_u32 v1, v4, v5
	v_mul_hi_u32 v1, v5, v1
	v_add_u32_e32 v1, v5, v1
	v_mul_hi_u32 v1, v6, v1
	v_mul_lo_u32 v4, v1, v3
	v_sub_u32_e32 v4, v6, v4
	v_add_u32_e32 v5, 1, v1
	v_cmp_ge_u32_e32 vcc, v4, v3
	s_nop 1
	v_cndmask_b32_e32 v1, v1, v5, vcc
	v_sub_u32_e32 v5, v4, v3
	v_cndmask_b32_e32 v4, v4, v5, vcc
	v_add_u32_e32 v5, 1, v1
	v_cmp_ge_u32_e32 vcc, v4, v3
	v_add_u32_e32 v4, 1, v6
	s_nop 0
	v_cndmask_b32_e32 v1, v1, v5, vcc
	v_mul_lo_u32 v5, v3, v1
	v_add_u32_e32 v3, v5, v3
	v_cmp_ne_u32_e32 vcc, v4, v3
	s_and_saveexec_b64 s[4:5], vcc
	s_xor_b64 s[28:29], exec, s[4:5]
	s_cbranch_execz .LBB0_101
	v_readlane_b32 s4, v254, 45
	v_readlane_b32 s5, v254, 46
	s_waitcnt lgkmcnt(0)
	s_nop 3
	global_load_dword v2, v115, s[4:5] sc1
	s_waitcnt vmcnt(0)
	v_cmp_eq_u32_e32 vcc, v2, v1
	s_and_saveexec_b64 s[38:39], vcc
	s_cbranch_execz .LBB0_100
	s_mov_b32 s4, 1
	s_mov_b64 s[40:41], 0
	s_branch .LBB0_91

.LBB0_100:
	s_or_b64 exec, exec, s[38:39]
	s_waitcnt vmcnt(0)
	s_waitcnt vmcnt(0)

.LBB0_118:
	s_or_b64 exec, exec, s[28:29]
	s_mov_b64 s[28:29], exec
	v_mbcnt_lo_u32_b32 v1, s28, 0
	v_mbcnt_hi_u32_b32 v1, s29, v1
	v_cmp_eq_u32_e32 vcc, 0, v1
	s_waitcnt vmcnt(0)
	s_and_saveexec_b64 s[38:39], vcc
	s_cbranch_execz .LBB0_120
	s_bcnt1_i32_b64 s4, s[28:29]
	v_mov_b32_e32 v1, s4
	v_readlane_b32 s4, v254, 45
	v_readlane_b32 s5, v254, 46
	s_nop 4
	global_atomic_add v115, v1, s[4:5]

.LBB0_238:
	s_or_b64 exec, exec, s[26:27]
	v_cvt_f32_u32_e32 v5, v3
	s_waitcnt vmcnt(0)
	buffer_inv sc1
	v_readfirstlane_b32 s4, v4
	v_sub_u32_e32 v4, 0, v3
	v_rcp_iflag_f32_e32 v5, v5
	v_add_u32_e32 v6, s4, v1
	v_mul_f32_e32 v5, 0x4f7ffffe, v5
	v_cvt_u32_f32_e32 v5, v5
	v_mul_lo_u32 v1, v4, v5
	v_mul_hi_u32 v1, v5, v1
	v_add_u32_e32 v1, v5, v1
	v_mul_hi_u32 v1, v6, v1
	v_mul_lo_u32 v4, v1, v3
	v_sub_u32_e32 v4, v6, v4
	v_add_u32_e32 v5, 1, v1
	v_cmp_ge_u32_e32 vcc, v4, v3
	s_nop 1
	v_cndmask_b32_e32 v1, v1, v5, vcc
	v_sub_u32_e32 v5, v4, v3
	v_cndmask_b32_e32 v4, v4, v5, vcc
	v_add_u32_e32 v5, 1, v1
	v_cmp_ge_u32_e32 vcc, v4, v3
	v_add_u32_e32 v4, 1, v6
	s_nop 0
	v_cndmask_b32_e32 v1, v1, v5, vcc
	v_mul_lo_u32 v5, v3, v1
	v_add_u32_e32 v3, v5, v3
	v_cmp_ne_u32_e32 vcc, v4, v3
	s_and_saveexec_b64 s[4:5], vcc
	s_xor_b64 s[26:27], exec, s[4:5]
	s_cbranch_execz .LBB0_252
	v_readlane_b32 s4, v254, 45
	v_readlane_b32 s5, v254, 46
	s_waitcnt lgkmcnt(0)
	s_nop 3
	global_load_dword v2, v115, s[4:5] sc1
	s_waitcnt vmcnt(0)
	v_cmp_eq_u32_e32 vcc, v2, v1
	s_and_saveexec_b64 s[28:29], vcc
	s_cbranch_execz .LBB0_251
	s_mov_b32 s4, 1
	s_mov_b64 s[38:39], 0
	s_branch .LBB0_242

.LBB0_251:
	s_or_b64 exec, exec, s[28:29]
	s_waitcnt vmcnt(0)
	s_waitcnt vmcnt(0)

.LBB0_269:
	s_or_b64 exec, exec, s[26:27]
	s_mov_b64 s[26:27], exec
	v_mbcnt_lo_u32_b32 v1, s26, 0
	v_mbcnt_hi_u32_b32 v1, s27, v1
	v_cmp_eq_u32_e32 vcc, 0, v1
	s_waitcnt vmcnt(0)
	s_and_saveexec_b64 s[28:29], vcc
	s_cbranch_execz .LBB0_271
	s_bcnt1_i32_b64 s4, s[26:27]
	v_mov_b32_e32 v1, s4
	v_readlane_b32 s4, v254, 45
	v_readlane_b32 s5, v254, 46
	s_nop 4
	global_atomic_add v115, v1, s[4:5]

.LBB0_413:
	s_or_b64 exec, exec, s[10:11]
	v_cvt_f32_u32_e32 v5, v3
	s_waitcnt vmcnt(0)
	buffer_inv sc1
	v_readfirstlane_b32 s4, v4
	v_sub_u32_e32 v4, 0, v3
	v_rcp_iflag_f32_e32 v5, v5
	v_add_u32_e32 v6, s4, v1
	v_mul_f32_e32 v5, 0x4f7ffffe, v5
	v_cvt_u32_f32_e32 v5, v5
	v_mul_lo_u32 v1, v4, v5
	v_mul_hi_u32 v1, v5, v1
	v_add_u32_e32 v1, v5, v1
	v_mul_hi_u32 v1, v6, v1
	v_mul_lo_u32 v4, v1, v3
	v_sub_u32_e32 v4, v6, v4
	v_add_u32_e32 v5, 1, v1
	v_cmp_ge_u32_e32 vcc, v4, v3
	s_nop 1
	v_cndmask_b32_e32 v1, v1, v5, vcc
	v_sub_u32_e32 v5, v4, v3
	v_cndmask_b32_e32 v4, v4, v5, vcc
	v_add_u32_e32 v5, 1, v1
	v_cmp_ge_u32_e32 vcc, v4, v3
	v_add_u32_e32 v4, 1, v6
	s_nop 0
	v_cndmask_b32_e32 v1, v1, v5, vcc
	v_mul_lo_u32 v5, v3, v1
	v_add_u32_e32 v3, v5, v3
	v_cmp_ne_u32_e32 vcc, v4, v3
	s_and_saveexec_b64 s[4:5], vcc
	s_xor_b64 s[10:11], exec, s[4:5]
	s_cbranch_execz .LBB0_427
	v_readlane_b32 s4, v254, 45
	v_readlane_b32 s5, v254, 46
	s_waitcnt lgkmcnt(0)
	s_nop 3
	global_load_dword v2, v115, s[4:5] sc1
	s_waitcnt vmcnt(0)
	v_cmp_eq_u32_e32 vcc, v2, v1
	s_and_saveexec_b64 s[26:27], vcc
	s_cbranch_execz .LBB0_426
	s_mov_b32 s4, 1
	s_mov_b64 s[28:29], 0
	s_branch .LBB0_417

.LBB0_426:
	s_or_b64 exec, exec, s[26:27]
	s_waitcnt vmcnt(0)
	s_waitcnt vmcnt(0)

.LBB0_444:
	s_or_b64 exec, exec, s[10:11]
	s_mov_b64 s[10:11], exec
	v_mbcnt_lo_u32_b32 v1, s10, 0
	v_mbcnt_hi_u32_b32 v1, s11, v1
	v_cmp_eq_u32_e32 vcc, 0, v1
	s_waitcnt vmcnt(0)
	s_and_saveexec_b64 s[26:27], vcc
	s_cbranch_execz .LBB0_446
	s_bcnt1_i32_b64 s4, s[10:11]
	v_mov_b32_e32 v1, s4
	v_readlane_b32 s4, v254, 45
	v_readlane_b32 s5, v254, 46
	s_nop 4
	global_atomic_add v115, v1, s[4:5]

.LBB0_569:
	s_or_b64 exec, exec, s[10:11]
	v_cvt_f32_u32_e32 v5, v3
	s_waitcnt vmcnt(0)
	buffer_inv sc1
	v_readfirstlane_b32 s4, v4
	v_sub_u32_e32 v4, 0, v3
	v_rcp_iflag_f32_e32 v5, v5
	v_add_u32_e32 v6, s4, v1
	v_mul_f32_e32 v5, 0x4f7ffffe, v5
	v_cvt_u32_f32_e32 v5, v5
	v_mul_lo_u32 v1, v4, v5
	v_mul_hi_u32 v1, v5, v1
	v_add_u32_e32 v1, v5, v1
	v_mul_hi_u32 v1, v6, v1
	v_mul_lo_u32 v4, v1, v3
	v_sub_u32_e32 v4, v6, v4
	v_add_u32_e32 v5, 1, v1
	v_cmp_ge_u32_e32 vcc, v4, v3
	s_nop 1
	v_cndmask_b32_e32 v1, v1, v5, vcc
	v_sub_u32_e32 v5, v4, v3
	v_cndmask_b32_e32 v4, v4, v5, vcc
	v_add_u32_e32 v5, 1, v1
	v_cmp_ge_u32_e32 vcc, v4, v3
	v_add_u32_e32 v4, 1, v6
	s_nop 0
	v_cndmask_b32_e32 v1, v1, v5, vcc
	v_mul_lo_u32 v5, v3, v1
	v_add_u32_e32 v3, v5, v3
	v_cmp_ne_u32_e32 vcc, v4, v3
	s_and_saveexec_b64 s[4:5], vcc
	s_xor_b64 s[10:11], exec, s[4:5]
	s_cbranch_execz .LBB0_583
	v_readlane_b32 s4, v254, 45
	v_readlane_b32 s5, v254, 46
	s_waitcnt lgkmcnt(0)
	s_nop 3
	global_load_dword v2, v115, s[4:5] sc1
	s_waitcnt vmcnt(0)
	v_cmp_eq_u32_e32 vcc, v2, v1
	s_and_saveexec_b64 s[28:29], vcc
	s_cbranch_execz .LBB0_582
	s_mov_b32 s4, 1
	s_mov_b64 s[38:39], 0
	s_branch .LBB0_573

.LBB0_600:
	s_or_b64 exec, exec, s[10:11]
	s_mov_b64 s[10:11], exec
	v_mbcnt_lo_u32_b32 v1, s10, 0
	v_mbcnt_hi_u32_b32 v1, s11, v1
	v_cmp_eq_u32_e32 vcc, 0, v1
	s_waitcnt vmcnt(0)
	s_and_saveexec_b64 s[28:29], vcc
	s_cbranch_execz .LBB0_602
	s_bcnt1_i32_b64 s4, s[10:11]
	v_mov_b32_e32 v1, s4
	v_readlane_b32 s4, v254, 45
	v_readlane_b32 s5, v254, 46
	s_nop 4
	global_atomic_add v115, v1, s[4:5]

.LBB0_1021:
	s_or_b64 exec, exec, s[4:5]
	v_cvt_f32_u32_e32 v5, v3
	s_waitcnt vmcnt(0)
	buffer_inv sc1
	v_readfirstlane_b32 s4, v4
	v_sub_u32_e32 v4, 0, v3
	v_rcp_iflag_f32_e32 v5, v5
	v_add_u32_e32 v6, s4, v1
	v_mul_f32_e32 v5, 0x4f7ffffe, v5
	v_cvt_u32_f32_e32 v5, v5
	v_mul_lo_u32 v1, v4, v5
	v_mul_hi_u32 v1, v5, v1
	v_add_u32_e32 v1, v5, v1
	v_mul_hi_u32 v1, v6, v1
	v_mul_lo_u32 v4, v1, v3
	v_sub_u32_e32 v4, v6, v4
	v_add_u32_e32 v5, 1, v1
	v_cmp_ge_u32_e32 vcc, v4, v3
	s_nop 1
	v_cndmask_b32_e32 v1, v1, v5, vcc
	v_sub_u32_e32 v5, v4, v3
	v_cndmask_b32_e32 v4, v4, v5, vcc
	v_add_u32_e32 v5, 1, v1
	v_cmp_ge_u32_e32 vcc, v4, v3
	v_add_u32_e32 v4, 1, v6
	s_nop 0
	v_cndmask_b32_e32 v1, v1, v5, vcc
	v_mul_lo_u32 v5, v3, v1
	v_add_u32_e32 v3, v5, v3
	v_cmp_ne_u32_e32 vcc, v4, v3
	s_and_saveexec_b64 s[4:5], vcc
	s_xor_b64 s[4:5], exec, s[4:5]
	s_cbranch_execz .LBB0_1035
	v_readlane_b32 s8, v254, 45
	v_readlane_b32 s9, v254, 46
	s_waitcnt lgkmcnt(0)
	s_nop 3
	global_load_dword v2, v115, s[8:9] sc1
	s_waitcnt vmcnt(0)
	v_cmp_eq_u32_e32 vcc, v2, v1
	s_and_saveexec_b64 s[8:9], vcc
	s_cbranch_execz .LBB0_1034
	s_mov_b32 s7, 1
	s_mov_b64 s[10:11], 0
	s_branch .LBB0_1025

.LBB0_1034:
	s_or_b64 exec, exec, s[8:9]
	s_waitcnt vmcnt(0)
	s_waitcnt vmcnt(0)

.LBB0_1052:
	s_or_b64 exec, exec, s[4:5]
	s_mov_b64 s[4:5], exec
	v_mbcnt_lo_u32_b32 v1, s4, 0
	v_mbcnt_hi_u32_b32 v1, s5, v1
	v_cmp_eq_u32_e32 vcc, 0, v1
	s_waitcnt vmcnt(0)
	s_and_saveexec_b64 s[8:9], vcc
	s_cbranch_execz .LBB0_1054
	s_bcnt1_i32_b64 s4, s[4:5]
	v_mov_b32_e32 v1, s4
	v_readlane_b32 s4, v254, 45
	v_readlane_b32 s5, v254, 46
	s_nop 4
	global_atomic_add v115, v1, s[4:5]

.LBB0_1124:
	s_or_b64 exec, exec, s[8:9]
	v_cvt_f32_u32_e32 v5, v3
	s_waitcnt vmcnt(0)
	buffer_inv sc1
	v_readfirstlane_b32 s7, v4
	v_sub_u32_e32 v4, 0, v3
	v_rcp_iflag_f32_e32 v5, v5
	v_add_u32_e32 v6, s7, v1
	v_mul_f32_e32 v5, 0x4f7ffffe, v5
	v_cvt_u32_f32_e32 v5, v5
	v_mul_lo_u32 v1, v4, v5
	v_mul_hi_u32 v1, v5, v1
	v_add_u32_e32 v1, v5, v1
	v_mul_hi_u32 v1, v6, v1
	v_mul_lo_u32 v4, v1, v3
	v_sub_u32_e32 v4, v6, v4
	v_add_u32_e32 v5, 1, v1
	v_cmp_ge_u32_e32 vcc, v4, v3
	s_nop 1
	v_cndmask_b32_e32 v1, v1, v5, vcc
	v_sub_u32_e32 v5, v4, v3
	v_cndmask_b32_e32 v4, v4, v5, vcc
	v_add_u32_e32 v5, 1, v1
	v_cmp_ge_u32_e32 vcc, v4, v3
	v_add_u32_e32 v4, 1, v6
	s_nop 0
	v_cndmask_b32_e32 v1, v1, v5, vcc
	v_mul_lo_u32 v5, v3, v1
	v_add_u32_e32 v3, v5, v3
	v_cmp_ne_u32_e32 vcc, v4, v3
	s_and_saveexec_b64 s[8:9], vcc
	s_xor_b64 s[8:9], exec, s[8:9]
	s_cbranch_execz .LBB0_1138
	v_readlane_b32 s10, v254, 45
	v_readlane_b32 s11, v254, 46
	s_waitcnt lgkmcnt(0)
	s_nop 3
	global_load_dword v2, v115, s[10:11] sc1
	s_waitcnt vmcnt(0)
	v_cmp_eq_u32_e32 vcc, v2, v1
	s_and_saveexec_b64 s[10:11], vcc
	s_cbranch_execz .LBB0_1137
	s_mov_b32 s7, 1
	s_mov_b64 s[26:27], 0
	s_branch .LBB0_1128

.LBB0_1137:
	s_or_b64 exec, exec, s[10:11]
	s_waitcnt vmcnt(0)
	s_waitcnt vmcnt(0)

.LBB0_1155:
	s_or_b64 exec, exec, s[8:9]
	s_mov_b64 s[8:9], exec
	v_mbcnt_lo_u32_b32 v1, s8, 0
	v_mbcnt_hi_u32_b32 v1, s9, v1
	v_cmp_eq_u32_e32 vcc, 0, v1
	s_waitcnt vmcnt(0)
	s_and_saveexec_b64 s[10:11], vcc
	s_cbranch_execz .LBB0_1157
	s_bcnt1_i32_b64 s7, s[8:9]
	v_readlane_b32 s8, v254, 45
	v_mov_b32_e32 v1, s7
	v_readlane_b32 s9, v254, 46
	s_nop 4
	global_atomic_add v115, v1, s[8:9]
